# P1 in-projection GEMM LDS tiles staged as full 128B lines (same layout change as P9/P10)
# baseline (speedup 1.0000x reference)
; #define PG8_STAGE(bufoff, gbase, voff) do { _Pragma("unroll") for (int _i = 0; _i < 2; ++_i) { unsigned _vo = (voff)[_i]; asm volatile("" : "+v"(_vo)); \
;         __builtin_amdgcn_global_load_lds((const unsigned*)((const char*)(gbase) + _vo), (LAS unsigned*)(lds + (bufoff) + ldsw + _i * 8192), 16, 0, 0); } } while (0)
; #define PG8_STAGE_A(bufoff, gbase, h, go) do { if constexpr (Sched::GATHER) { PG8_STAGE(bufoff, gbase, go[h]); } else { PG8_STAGE(bufoff, (gbase) + (h) * hstep, voffA); } } while (0)
; #define PG8_WAIT_V(n) asm volatile("s_waitcnt vmcnt(" #n ")" ::: "memory")
; #define PG8_BAR __builtin_amdgcn_s_barrier()
;     __device__ __forceinline__ void prefetch(const Unit& u) const { if (u.e == 0) rs.prefetch(u); else cs.prefetch(u); }
;     ...
;     for (int i = 0; i < 2; ++i) { int R, C; stage_rc(tid * 16 + i * 8192, R, C); const int Rb = Epi::PERM ? ((R & ~31) + perm32(R & 31)) : R;
;         voffA[i] = Sched::GATHER ? (unsigned)(C * 2) : (unsigned)(R * KB + C * 2); voffB[i] = (unsigned)(Rb * KB + C * 2); }
;     const size_t kstep = (size_t)(BK * 2);
;     const size_t hstep = (size_t)HALF * KB;
;     const unsigned ldsw = (unsigned)wid * 1024u;
;     const int aoff = lds_byte(wr * 64 + fr, fq * 8), boff = lds_byte(wc * 32 + fr, fq * 8);
;     ...
;     Unit cur, nxt; int ui = 0;
;     if (!S.next(0, cur)) return;
;     Acc acc;
; #pragma unroll
;     for (int a = 0; a < 2; ++a)
; #pragma unroll
;         for (int b = 0; b < 2; ++b)
; #pragma unroll
;             for (int m = 0; m < 4; ++m)
; #pragma unroll
;                 for (int n = 0; n < 2; ++n) acc[a][b][m][n] = (f32x4){0.f, 0.f, 0.f, 0.f};
;     bf16x8 At[4][2], B0[2][2], B1[2][2];
;     const char* cA = cur.a; const char* cB = cur.b;
;     unsigned gc[2][2], gn[2][2];
;     if constexpr (Sched::GATHER) { S.gather(cur, voffA, gc); }
;     if constexpr (Epi::PREF) E.prefetch(cur);
;     PG8_STAGE(PG8_SB(0, 0), cB, voffB); PG8_STAGE(PG8_SB(0, 1), cB + hstep, voffB); PG8_STAGE_A(PG8_SA(0, 0), cA, 0, gc); PG8_STAGE_A(PG8_SA(0, 1), cA, 1, gc);
;     if (wr == 1) PG8_BAR;
;     PG8_WAIT_V(2); PG8_BAR;
;     PG8_STAGE(PG8_SB(1, 0), cB + kstep, voffB); PG8_STAGE_A(PG8_SA(1, 0), cA + kstep, 0, gc); PG8_STAGE(PG8_SB(1, 1), cB + hstep + kstep, voffB);
;     PG8_WAIT_V(6); PG8_BAR;
.LBB5_786:
	v_lshrrev_b32_e32 v1, 4, v0
	s_waitcnt vmcnt(0)
	v_xor_b32_e32 v1, v1, v0
	v_and_b32_e32 v1, 7, v1
	v_lshlrev_b32_e32 v2, 4, v1
	v_lshrrev_b32_e32 v5, 3, v0
	v_and_b32_e32 v4, 0x23, v5
	v_and_b32_e32 v6, 12, v5
	v_lshl_or_b32 v4, v6, 1, v4
	v_bfe_u32 v6, v5, 4, 1
	v_lshl_or_b32 v6, v6, 2, v4
	v_lshl_or_b32 v1, v5, 12, v2
	v_or_b32_e32 v3, 64, v5
	s_movk_i32 s8, 0x70
	s_lshr_b32 s12, s18, 6
	s_movk_i32 s8, 0x60
	v_lshl_or_b32 v162, v6, 12, v2
	v_or_b32_e32 v4, 64, v6
	s_lshl_b32 s17, s12, 10
	v_lshl_or_b32 v163, v3, 12, v2
	v_lshl_or_b32 v164, v4, 12, v2
	s_add_i32 s29, s17, 0
	v_mov_b32_e32 v2, v162
	s_add_i32 m0, s29, 0x10000
	s_lshr_b32 s34, s18, 8
	global_load_lds_dwordx4 v2, s[4:5]
	v_mov_b32_e32 v2, v164
	s_add_i32 m0, s29, 0x12000
	s_add_u32 s8, s4, 0x80000
	global_load_lds_dwordx4 v2, s[4:5]
	v_mov_b32_e32 v2, v162
	s_addc_u32 s9, s5, 0
	s_add_i32 m0, s29, 0x14000
	s_add_i32 s35, s29, 0x2000
	global_load_lds_dwordx4 v2, s[8:9]
	v_mov_b32_e32 v2, v164
	s_add_i32 m0, s29, 0x16000
	s_mov_b32 s75, 0
	global_load_lds_dwordx4 v2, s[8:9]
	v_mov_b32_e32 v2, v1
	s_mov_b32 m0, s29
	s_add_u32 s8, s0, 0x80000
	global_load_lds_dwordx4 v2, s[0:1]
	v_mov_b32_e32 v2, v163
	s_mov_b32 m0, s35
	s_addc_u32 s9, s1, 0
	global_load_lds_dwordx4 v2, s[0:1]
	s_add_i32 s37, s29, 0x4000
	v_mov_b32_e32 v2, v1
	s_mov_b32 m0, s37
	s_add_i32 s55, s29, 0x6000
	global_load_lds_dwordx4 v2, s[8:9]
	v_mov_b32_e32 v2, v163
	s_mov_b32 m0, s55
	s_cmp_eq_u32 s34, 1
	global_load_lds_dwordx4 v2, s[8:9]
	s_cselect_b64 s[8:9], -1, 0
	s_cmp_lg_u32 s34, 1
	s_cbranch_scc1 .LBB5_788
	s_barrier
.LBB5_788:
	s_add_u32 s60, s22, 2.0
	s_addc_u32 s61, s23, 0
	s_add_u32 s10, s22, 0x50000000
	v_mov_b32_e32 v138, v162
	v_mov_b32_e32 v139, 0
	s_addc_u32 s11, s23, 0
	s_and_b32 s36, s12, 3
	s_waitcnt vmcnt(2)
	s_barrier
	s_mov_b64 s[12:13], 0x80
	v_lshl_add_u64 v[2:3], s[4:5], 0, v[138:139]
	s_add_i32 m0, s29, 0x18000
	v_lshl_add_u64 v[2:3], v[2:3], 0, s[12:13]
	v_mov_b32_e32 v138, v164
	global_load_lds_dwordx4 v[2:3], off
	s_add_i32 m0, s29, 0x1a000
	v_lshl_add_u64 v[2:3], s[4:5], 0, v[138:139]
	v_lshl_add_u64 v[2:3], v[2:3], 0, s[12:13]
	v_mov_b32_e32 v138, v1
	global_load_lds_dwordx4 v[2:3], off
	s_add_i32 s64, s29, 0x8000
	v_lshl_add_u64 v[2:3], s[0:1], 0, v[138:139]
	v_lshl_add_u64 v[2:3], v[2:3], 0, s[12:13]
	s_mov_b32 m0, s64
	v_mov_b32_e32 v138, v163
	global_load_lds_dwordx4 v[2:3], off
	s_add_i32 s65, s29, 0xa000
	v_lshl_add_u64 v[2:3], s[0:1], 0, v[138:139]
	s_lshl_b32 s62, s34, 6
	s_lshl_b32 s19, s34, 13
	s_lshl_b32 s63, s36, 5
	s_lshl_b32 s40, s36, 12
	v_lshl_add_u64 v[2:3], v[2:3], 0, s[12:13]
	s_mov_b32 m0, s65
	s_add_u32 s38, s4, 0x80080
	global_load_lds_dwordx4 v[2:3], off
	v_mov_b32_e32 v2, v162
	s_addc_u32 s39, s5, 0
	s_add_i32 m0, s29, 0x1c000
	v_bfe_u32 v166, v0, 4, 2
	global_load_lds_dwordx4 v2, s[38:39]
	v_mov_b32_e32 v2, v164
	s_add_i32 m0, s29, 0x1e000
	v_and_b32_e32 v165, 15, v0
	global_load_lds_dwordx4 v2, s[38:39]
	v_lshrrev_b32_e32 v3, 1, v165
	v_lshlrev_b32_e32 v2, 2, v0
	v_xor_b32_e32 v3, v3, v166
	v_lshlrev_b32_e32 v3, 4, v3
	v_lshl_or_b32 v3, v165, 7, v3
	v_or_b32_e32 v4, s19, v3
	s_movk_i32 s19, 0x3c0
	s_waitcnt vmcnt(6)
	s_cmpk_lt_u32 s18, 0x100
	v_or_b32_e32 v167, s40, v3
	s_cselect_b64 s[18:19], -1, 0
	s_lshl_b32 s36, s36, 7
	s_add_i32 s67, 0, 0x20800
	s_lshl_b32 s34, s34, 8
	v_mov_b32_e32 v3, v139
	s_add_i32 s68, 0, 0x10000
	s_add_i32 s69, 0, 0x14000
	s_add_i32 s66, s67, s36
	s_add_i32 s67, s67, s34
	v_lshl_add_u64 v[140:141], s[6:7], 0, v[2:3]
	v_add_u32_e32 v168, s68, v167
	v_add_u32_e32 v169, s69, v167
	v_add_u32_e32 v170, 0, v4
	s_mov_b32 s34, 0x3a000000
	s_mov_b32 s70, 0x800000
	s_mov_b32 s36, 0x45800000
	v_mov_b32_e32 v171, 0x358637bd
	v_mov_b32_e32 v172, 0x3e38aa3b
	s_mov_b32 s71, 0
	s_mov_b64 s[42:43], s[4:5]
	s_mov_b64 s[40:41], s[0:1]
	s_barrier
	s_branch .LBB5_791

; #define PG8_STAGE(bufoff, gbase, voff) do { _Pragma("unroll") for (int _i = 0; _i < 2; ++_i) { unsigned _vo = (voff)[_i]; asm volatile("" : "+v"(_vo)); \
;         __builtin_amdgcn_global_load_lds((const unsigned*)((const char*)(gbase) + _vo), (LAS unsigned*)(lds + (bufoff) + ldsw + _i * 8192), 16, 0, 0); } } while (0)
; #define PG8_STAGE_A(bufoff, gbase, h, go) do { if constexpr (Sched::GATHER) { PG8_STAGE(bufoff, gbase, go[h]); } else { PG8_STAGE(bufoff, (gbase) + (h) * hstep, voffA); } } while (0)
; #define PG8_LDA(dst, b, h) do { _Pragma("unroll") for (int m = 0; m < 4; ++m) _Pragma("unroll") for (int k = 0; k < 2; ++k) dst[m][k] = *(const LAS bf16x8*)(lds + PG8_SA(b, h) + aoff + m * 2048 + k * 1024); } while (0)
; #define PG8_LDB(dst, b, h) do { _Pragma("unroll") for (int n = 0; n < 2; ++n) _Pragma("unroll") for (int k = 0; k < 2; ++k) dst[n][k] = *(const LAS bf16x8*)(lds + PG8_SB(b, h) + boff + n * 2048 + k * 1024); } while (0)
; #define PG8_WAIT_V(n) asm volatile("s_waitcnt vmcnt(" #n ")" ::: "memory")
; #define PG8_WAIT_L(n) asm volatile("s_waitcnt lgkmcnt(" #n ")" ::: "memory")
; #define PG8_BAR __builtin_amdgcn_s_barrier()
; #define PG8_SCHED __builtin_amdgcn_sched_barrier(0)
;     ...
;             PG8_LDB(B0, 0, 0); PG8_LDB(B1, 0, 1); PG8_SCHED; PG8_LDA(At, 0, 0); PG8_STAGE_A(PG8_SA(1, 1), a1, 1, gc);
;             if constexpr (Sched::GATHER) { if (last) {
; #pragma unroll
;                 for (int h = 0; h < 2; ++h)
; #pragma unroll
;                     for (int i = 0; i < 2; ++i) gc[h][i] = gn[h][i]; } }
;             PG8_WAIT_V(8); PG8_WAIT_L(0); PG8_BAR; PG8_MMA(0, 0, At, B0); PG8_MMA(0, 1, At, B1); PG8_BAR; PG8_SCHED;
;             PG8_LDA(At, 0, 1); PG8_STAGE(PG8_SB(0, 0), b2, voffB); PG8_STAGE(PG8_SB(0, 1), b2 + hstep, voffB); PG8_STAGE_A(PG8_SA(0, 0), a2, 0, gc);
;             PG8_WAIT_V(8); PG8_WAIT_L(0); PG8_BAR; PG8_MMA(1, 0, At, B0); PG8_MMA(1, 1, At, B1); PG8_BAR; PG8_SCHED;
.LBB5_802:
	ds_read_b128 v[130:133], v168
	ds_read_b128 v[142:145], v168 offset:2048
	v_xor_b32_e32 v168, 64, v168
	ds_read_b128 v[134:137], v168
	ds_read_b128 v[146:149], v168 offset:2048
	v_xor_b32_e32 v168, 64, v168
	ds_read_b128 v[150:153], v169
	ds_read_b128 v[158:161], v169 offset:2048
	v_xor_b32_e32 v169, 64, v169
	ds_read_b128 v[154:157], v169
	ds_read_b128 v[174:177], v169 offset:2048
	v_xor_b32_e32 v169, 64, v169
	s_add_u32 s4, s0, 0xfff80080
	s_addc_u32 s5, s1, -1
	s_cmp_eq_u32 s79, 28
	s_cselect_b32 s5, s41, s5
	s_cselect_b32 s4, s40, s4
	s_cselect_b32 s7, s43, s78
	s_cselect_b32 s6, s42, s77
	v_mov_b32_e32 v138, v1
	ds_read_b128 v[178:181], v170
	ds_read_b128 v[186:189], v170 offset:2048
	ds_read_b128 v[194:197], v170 offset:4096
	ds_read_b128 v[204:207], v170 offset:6144
	v_xor_b32_e32 v170, 64, v170
	ds_read_b128 v[182:185], v170
	ds_read_b128 v[190:193], v170 offset:2048
	ds_read_b128 v[200:203], v170 offset:4096
	ds_read_b128 v[208:211], v170 offset:6144
	s_add_i32 m0, s29, 0xc000
	s_nop 0
	global_load_lds_dwordx4 v138, s[0:1]
	v_mov_b32_e32 v138, v163
	s_add_i32 m0, s29, 0xe000
	s_nop 0
	global_load_lds_dwordx4 v138, s[0:1]
	s_waitcnt vmcnt(8)
	s_waitcnt lgkmcnt(0)
	s_barrier
	s_setprio 1
	s_waitcnt lgkmcnt(0)
	v_mfma_f32_16x16x32_bf16 v[126:129], v[130:133], v[178:181], v[126:129]
	v_mfma_f32_16x16x32_bf16 v[122:125], v[142:145], v[178:181], v[122:125]
	v_mfma_f32_16x16x32_bf16 v[110:113], v[130:133], v[186:189], v[110:113]
	v_mfma_f32_16x16x32_bf16 v[106:109], v[142:145], v[186:189], v[106:109]
	v_mfma_f32_16x16x32_bf16 v[94:97], v[130:133], v[194:197], v[94:97]
	v_mfma_f32_16x16x32_bf16 v[90:93], v[142:145], v[194:197], v[90:93]
	v_mfma_f32_16x16x32_bf16 v[78:81], v[130:133], v[204:207], v[78:81]
	v_mfma_f32_16x16x32_bf16 v[74:77], v[142:145], v[204:207], v[74:77]
	v_mfma_f32_16x16x32_bf16 v[126:129], v[134:137], v[182:185], v[126:129]
	v_mfma_f32_16x16x32_bf16 v[122:125], v[146:149], v[182:185], v[122:125]
	v_mfma_f32_16x16x32_bf16 v[110:113], v[134:137], v[190:193], v[110:113]
	v_mfma_f32_16x16x32_bf16 v[106:109], v[146:149], v[190:193], v[106:109]
	v_mfma_f32_16x16x32_bf16 v[94:97], v[134:137], v[200:203], v[94:97]
	v_mfma_f32_16x16x32_bf16 v[90:93], v[146:149], v[200:203], v[90:93]
	v_mfma_f32_16x16x32_bf16 v[78:81], v[134:137], v[208:211], v[78:81]
	v_mfma_f32_16x16x32_bf16 v[74:77], v[146:149], v[208:211], v[74:77]
	s_setprio 0
	s_setprio 1
	v_mfma_f32_16x16x32_bf16 v[118:121], v[150:153], v[178:181], v[118:121]
	v_mfma_f32_16x16x32_bf16 v[114:117], v[158:161], v[178:181], v[114:117]
	v_mfma_f32_16x16x32_bf16 v[102:105], v[150:153], v[186:189], v[102:105]
	v_mfma_f32_16x16x32_bf16 v[98:101], v[158:161], v[186:189], v[98:101]
	v_mfma_f32_16x16x32_bf16 v[86:89], v[150:153], v[194:197], v[86:89]
	v_mfma_f32_16x16x32_bf16 v[82:85], v[158:161], v[194:197], v[82:85]
	v_mfma_f32_16x16x32_bf16 v[70:73], v[150:153], v[204:207], v[70:73]
	v_mfma_f32_16x16x32_bf16 v[66:69], v[158:161], v[204:207], v[66:69]
	v_mfma_f32_16x16x32_bf16 v[118:121], v[154:157], v[182:185], v[118:121]
	v_mfma_f32_16x16x32_bf16 v[114:117], v[174:177], v[182:185], v[114:117]
	v_mfma_f32_16x16x32_bf16 v[102:105], v[154:157], v[190:193], v[102:105]
	v_mfma_f32_16x16x32_bf16 v[98:101], v[174:177], v[190:193], v[98:101]
	v_mfma_f32_16x16x32_bf16 v[86:89], v[154:157], v[200:203], v[86:89]
	v_mfma_f32_16x16x32_bf16 v[82:85], v[174:177], v[200:203], v[82:85]
	v_mfma_f32_16x16x32_bf16 v[70:73], v[154:157], v[208:211], v[70:73]
	v_mfma_f32_16x16x32_bf16 v[66:69], v[174:177], v[208:211], v[66:69]
	s_setprio 0
	s_barrier
	v_mov_b32_e32 v138, v162
	s_add_i32 s80, s68, s17
	ds_read_b128 v[182:185], v170 offset:16384
	ds_read_b128 v[190:193], v170 offset:18432
	ds_read_b128 v[200:203], v170 offset:20480
	ds_read_b128 v[208:211], v170 offset:22528
	v_xor_b32_e32 v170, 64, v170
	ds_read_b128 v[178:181], v170 offset:16384
	ds_read_b128 v[186:189], v170 offset:18432
	ds_read_b128 v[194:197], v170 offset:20480
	ds_read_b128 v[204:207], v170 offset:22528
	s_mov_b32 m0, s80
	s_nop 0
	global_load_lds_dwordx4 v138, s[6:7]
	v_mov_b32_e32 v138, v164
	s_add_i32 m0, s80, 0x2000
	s_add_u32 s80, s6, 0x80000
	global_load_lds_dwordx4 v138, s[6:7]
	s_addc_u32 s81, s7, 0
	v_mov_b32_e32 v138, v162
	s_add_i32 s82, s69, s17
	s_mov_b32 m0, s82
	s_nop 0
	global_load_lds_dwordx4 v138, s[80:81]
	v_mov_b32_e32 v138, v164
	s_add_i32 m0, s82, 0x2000
	s_nop 0
	global_load_lds_dwordx4 v138, s[80:81]
	v_mov_b32_e32 v138, v1
	s_mov_b32 m0, s29
	s_nop 0
	global_load_lds_dwordx4 v138, s[4:5]
	v_mov_b32_e32 v138, v163
	s_mov_b32 m0, s35
	s_nop 0
	global_load_lds_dwordx4 v138, s[4:5]
	s_waitcnt vmcnt(8)
	s_waitcnt lgkmcnt(0)
	s_barrier
; #define PG8_STAGE(bufoff, gbase, voff) do { _Pragma("unroll") for (int _i = 0; _i < 2; ++_i) { unsigned _vo = (voff)[_i]; asm volatile("" : "+v"(_vo)); \
;         __builtin_amdgcn_global_load_lds((const unsigned*)((const char*)(gbase) + _vo), (LAS unsigned*)(lds + (bufoff) + ldsw + _i * 8192), 16, 0, 0); } } while (0)
; #define PG8_STAGE_A(bufoff, gbase, h, go) do { if constexpr (Sched::GATHER) { PG8_STAGE(bufoff, gbase, go[h]); } else { PG8_STAGE(bufoff, (gbase) + (h) * hstep, voffA); } } while (0)
; #define PG8_LDA(dst, b, h) do { _Pragma("unroll") for (int m = 0; m < 4; ++m) _Pragma("unroll") for (int k = 0; k < 2; ++k) dst[m][k] = *(const LAS bf16x8*)(lds + PG8_SA(b, h) + aoff + m * 2048 + k * 1024); } while (0)
; #define PG8_LDB(dst, b, h) do { _Pragma("unroll") for (int n = 0; n < 2; ++n) _Pragma("unroll") for (int k = 0; k < 2; ++k) dst[n][k] = *(const LAS bf16x8*)(lds + PG8_SB(b, h) + boff + n * 2048 + k * 1024); } while (0)
; #define PG8_WAIT_V(n) asm volatile("s_waitcnt vmcnt(" #n ")" ::: "memory")
; #define PG8_WAIT_L(n) asm volatile("s_waitcnt lgkmcnt(" #n ")" ::: "memory")
; #define PG8_BAR __builtin_amdgcn_s_barrier()
; #define PG8_SCHED __builtin_amdgcn_sched_barrier(0)
;     ...
;             PG8_WAIT_V(8); PG8_WAIT_L(0); PG8_BAR; PG8_MMA(0, 0, At, B0); PG8_MMA(0, 1, At, B1); PG8_BAR; PG8_SCHED;
;             PG8_LDA(At, 0, 1); PG8_STAGE(PG8_SB(0, 0), b2, voffB); PG8_STAGE(PG8_SB(0, 1), b2 + hstep, voffB); PG8_STAGE_A(PG8_SA(0, 0), a2, 0, gc);
;             PG8_WAIT_V(8); PG8_WAIT_L(0); PG8_BAR; PG8_MMA(1, 0, At, B0); PG8_MMA(1, 1, At, B1); PG8_BAR; PG8_SCHED;
;             PG8_LDB(B0, 1, 0); PG8_LDB(B1, 1, 1); PG8_SCHED; PG8_LDA(At, 1, 0); PG8_STAGE_A(PG8_SA(0, 1), a2, 1, gc);
;             PG8_WAIT_V(8); PG8_WAIT_L(0); PG8_BAR; PG8_MMA(0, 0, At, B0); PG8_MMA(0, 1, At, B1); PG8_BAR; PG8_SCHED;
	s_setprio 1
	s_waitcnt lgkmcnt(0)
	v_mfma_f32_16x16x32_bf16 v[62:65], v[130:133], v[178:181], v[62:65]
	v_mfma_f32_16x16x32_bf16 v[58:61], v[142:145], v[178:181], v[58:61]
	v_mfma_f32_16x16x32_bf16 v[46:49], v[130:133], v[186:189], v[46:49]
	v_mfma_f32_16x16x32_bf16 v[42:45], v[142:145], v[186:189], v[42:45]
	v_mfma_f32_16x16x32_bf16 v[30:33], v[130:133], v[194:197], v[30:33]
	v_mfma_f32_16x16x32_bf16 v[26:29], v[142:145], v[194:197], v[26:29]
	v_mfma_f32_16x16x32_bf16 v[14:17], v[130:133], v[204:207], v[14:17]
	v_mfma_f32_16x16x32_bf16 v[10:13], v[142:145], v[204:207], v[10:13]
	v_mfma_f32_16x16x32_bf16 v[62:65], v[134:137], v[182:185], v[62:65]
	v_mfma_f32_16x16x32_bf16 v[58:61], v[146:149], v[182:185], v[58:61]
	v_mfma_f32_16x16x32_bf16 v[46:49], v[134:137], v[190:193], v[46:49]
	v_mfma_f32_16x16x32_bf16 v[42:45], v[146:149], v[190:193], v[42:45]
	v_mfma_f32_16x16x32_bf16 v[30:33], v[134:137], v[200:203], v[30:33]
	v_mfma_f32_16x16x32_bf16 v[26:29], v[146:149], v[200:203], v[26:29]
	v_mfma_f32_16x16x32_bf16 v[14:17], v[134:137], v[208:211], v[14:17]
	v_mfma_f32_16x16x32_bf16 v[10:13], v[146:149], v[208:211], v[10:13]
	s_setprio 0
	s_setprio 1
	v_mfma_f32_16x16x32_bf16 v[54:57], v[150:153], v[178:181], v[54:57]
	v_mfma_f32_16x16x32_bf16 v[50:53], v[158:161], v[178:181], v[50:53]
	v_mfma_f32_16x16x32_bf16 v[38:41], v[150:153], v[186:189], v[38:41]
	v_mfma_f32_16x16x32_bf16 v[34:37], v[158:161], v[186:189], v[34:37]
	v_mfma_f32_16x16x32_bf16 v[22:25], v[150:153], v[194:197], v[22:25]
	v_mfma_f32_16x16x32_bf16 v[18:21], v[158:161], v[194:197], v[18:21]
	v_mfma_f32_16x16x32_bf16 v[6:9], v[150:153], v[204:207], v[6:9]
	v_mfma_f32_16x16x32_bf16 v[2:5], v[158:161], v[204:207], v[2:5]
	v_mfma_f32_16x16x32_bf16 v[54:57], v[154:157], v[182:185], v[54:57]
	v_mfma_f32_16x16x32_bf16 v[50:53], v[174:177], v[182:185], v[50:53]
	v_mfma_f32_16x16x32_bf16 v[38:41], v[154:157], v[190:193], v[38:41]
	v_mfma_f32_16x16x32_bf16 v[34:37], v[174:177], v[190:193], v[34:37]
	v_mfma_f32_16x16x32_bf16 v[22:25], v[154:157], v[200:203], v[22:25]
	v_mfma_f32_16x16x32_bf16 v[18:21], v[174:177], v[200:203], v[18:21]
	v_mfma_f32_16x16x32_bf16 v[6:9], v[154:157], v[208:211], v[6:9]
	v_mfma_f32_16x16x32_bf16 v[2:5], v[174:177], v[208:211], v[2:5]
	s_setprio 0
	s_barrier
	s_add_i32 s82, 0, 0x18000
	v_add_u32_e32 v138, s82, v167
	s_add_i32 s83, 0, 0x1c000
	ds_read_b128 v[130:133], v138
	ds_read_b128 v[142:145], v138 offset:2048
	v_xor_b32_e32 v138, 64, v138
	ds_read_b128 v[134:137], v138
	ds_read_b128 v[146:149], v138 offset:2048
	v_add_u32_e32 v138, s83, v167
	ds_read_b128 v[150:153], v138
	ds_read_b128 v[158:161], v138 offset:2048
	v_xor_b32_e32 v138, 64, v138
	ds_read_b128 v[154:157], v138
	ds_read_b128 v[174:177], v138 offset:2048
	s_add_u32 s80, s4, 0x80000
	v_mov_b32_e32 v138, v1
	s_mov_b32 m0, s37
	ds_read_b128 v[178:181], v170 offset:32768
	ds_read_b128 v[186:189], v170 offset:34816
	ds_read_b128 v[194:197], v170 offset:36864
	ds_read_b128 v[204:207], v170 offset:38912
	v_xor_b32_e32 v170, 64, v170
	ds_read_b128 v[182:185], v170 offset:32768
	ds_read_b128 v[190:193], v170 offset:34816
	ds_read_b128 v[200:203], v170 offset:36864
	ds_read_b128 v[208:211], v170 offset:38912
	s_addc_u32 s81, s5, 0
	s_nop 0
	global_load_lds_dwordx4 v138, s[80:81]
	v_mov_b32_e32 v138, v163
	s_mov_b32 m0, s55
	s_nop 0
	global_load_lds_dwordx4 v138, s[80:81]
	s_waitcnt vmcnt(8)
	s_waitcnt lgkmcnt(0)
	s_barrier
	s_setprio 1
	s_waitcnt lgkmcnt(0)
	v_mfma_f32_16x16x32_bf16 v[126:129], v[130:133], v[178:181], v[126:129]
	v_mfma_f32_16x16x32_bf16 v[122:125], v[142:145], v[178:181], v[122:125]
	v_mfma_f32_16x16x32_bf16 v[110:113], v[130:133], v[186:189], v[110:113]
	v_mfma_f32_16x16x32_bf16 v[106:109], v[142:145], v[186:189], v[106:109]
	v_mfma_f32_16x16x32_bf16 v[94:97], v[130:133], v[194:197], v[94:97]
	v_mfma_f32_16x16x32_bf16 v[90:93], v[142:145], v[194:197], v[90:93]
	v_mfma_f32_16x16x32_bf16 v[78:81], v[130:133], v[204:207], v[78:81]
	v_mfma_f32_16x16x32_bf16 v[74:77], v[142:145], v[204:207], v[74:77]
	v_mfma_f32_16x16x32_bf16 v[126:129], v[134:137], v[182:185], v[126:129]
	v_mfma_f32_16x16x32_bf16 v[122:125], v[146:149], v[182:185], v[122:125]
	v_mfma_f32_16x16x32_bf16 v[110:113], v[134:137], v[190:193], v[110:113]
	v_mfma_f32_16x16x32_bf16 v[106:109], v[146:149], v[190:193], v[106:109]
	v_mfma_f32_16x16x32_bf16 v[94:97], v[134:137], v[200:203], v[94:97]
	v_mfma_f32_16x16x32_bf16 v[90:93], v[146:149], v[200:203], v[90:93]
	v_mfma_f32_16x16x32_bf16 v[78:81], v[134:137], v[208:211], v[78:81]
	v_mfma_f32_16x16x32_bf16 v[74:77], v[146:149], v[208:211], v[74:77]
	s_setprio 0
	s_setprio 1
	v_mfma_f32_16x16x32_bf16 v[118:121], v[150:153], v[178:181], v[118:121]
	v_mfma_f32_16x16x32_bf16 v[114:117], v[158:161], v[178:181], v[114:117]
	v_mfma_f32_16x16x32_bf16 v[102:105], v[150:153], v[186:189], v[102:105]
	v_mfma_f32_16x16x32_bf16 v[98:101], v[158:161], v[186:189], v[98:101]
	v_mfma_f32_16x16x32_bf16 v[86:89], v[150:153], v[194:197], v[86:89]
	v_mfma_f32_16x16x32_bf16 v[82:85], v[158:161], v[194:197], v[82:85]
	v_mfma_f32_16x16x32_bf16 v[70:73], v[150:153], v[204:207], v[70:73]
	v_mfma_f32_16x16x32_bf16 v[66:69], v[158:161], v[204:207], v[66:69]
	v_mfma_f32_16x16x32_bf16 v[118:121], v[154:157], v[182:185], v[118:121]
	v_mfma_f32_16x16x32_bf16 v[114:117], v[174:177], v[182:185], v[114:117]
	v_mfma_f32_16x16x32_bf16 v[102:105], v[154:157], v[190:193], v[102:105]
	v_mfma_f32_16x16x32_bf16 v[98:101], v[174:177], v[190:193], v[98:101]
	v_mfma_f32_16x16x32_bf16 v[86:89], v[154:157], v[200:203], v[86:89]
	v_mfma_f32_16x16x32_bf16 v[82:85], v[174:177], v[200:203], v[82:85]
	v_mfma_f32_16x16x32_bf16 v[70:73], v[154:157], v[208:211], v[70:73]
	v_mfma_f32_16x16x32_bf16 v[66:69], v[174:177], v[208:211], v[66:69]
	s_setprio 0
	s_barrier
; #define PG8_STAGE(bufoff, gbase, voff) do { _Pragma("unroll") for (int _i = 0; _i < 2; ++_i) { unsigned _vo = (voff)[_i]; asm volatile("" : "+v"(_vo)); \
;         __builtin_amdgcn_global_load_lds((const unsigned*)((const char*)(gbase) + _vo), (LAS unsigned*)(lds + (bufoff) + ldsw + _i * 8192), 16, 0, 0); } } while (0)
; #define PG8_STAGE_A(bufoff, gbase, h, go) do { if constexpr (Sched::GATHER) { PG8_STAGE(bufoff, gbase, go[h]); } else { PG8_STAGE(bufoff, (gbase) + (h) * hstep, voffA); } } while (0)
; #define PG8_LDA(dst, b, h) do { _Pragma("unroll") for (int m = 0; m < 4; ++m) _Pragma("unroll") for (int k = 0; k < 2; ++k) dst[m][k] = *(const LAS bf16x8*)(lds + PG8_SA(b, h) + aoff + m * 2048 + k * 1024); } while (0)
; #define PG8_WAIT_V(n) asm volatile("s_waitcnt vmcnt(" #n ")" ::: "memory")
; #define PG8_WAIT_L(n) asm volatile("s_waitcnt lgkmcnt(" #n ")" ::: "memory")
; #define PG8_BAR __builtin_amdgcn_s_barrier()
; #define PG8_SCHED __builtin_amdgcn_sched_barrier(0)
;     ...
;             PG8_LDA(At, 1, 1); PG8_STAGE(PG8_SB(1, 0), b3, voffB); PG8_STAGE(PG8_SB(1, 1), b3 + hstep, voffB); PG8_STAGE_A(PG8_SA(1, 0), a3, 0, gc);
;             PG8_WAIT_V(8); PG8_WAIT_L(0); PG8_BAR; PG8_MMA(1, 0, At, B0); PG8_MMA(1, 1, At, B1); PG8_BAR; PG8_SCHED;
;         }
	v_mov_b32_e32 v138, v162
	ds_read_b128 v[182:185], v170 offset:49152
	ds_read_b128 v[190:193], v170 offset:51200
	ds_read_b128 v[200:203], v170 offset:53248
	ds_read_b128 v[208:211], v170 offset:55296
	v_xor_b32_e32 v170, 64, v170
	ds_read_b128 v[178:181], v170 offset:49152
	ds_read_b128 v[186:189], v170 offset:51200
	ds_read_b128 v[194:197], v170 offset:53248
	ds_read_b128 v[204:207], v170 offset:55296
	s_add_i32 s80, s82, s17
	v_lshl_add_u64 v[214:215], s[6:7], 0, v[138:139]
	v_lshl_add_u64 v[214:215], v[214:215], 0, s[12:13]
	s_mov_b32 m0, s80
	v_mov_b32_e32 v138, v164
	global_load_lds_dwordx4 v[214:215], off
	s_add_i32 m0, s80, 0x2000
	s_nop 0
	v_lshl_add_u64 v[214:215], s[6:7], 0, v[138:139]
	s_add_u32 s6, s6, 0x80080
	v_lshl_add_u64 v[214:215], v[214:215], 0, s[12:13]
	s_addc_u32 s7, s7, 0
	v_mov_b32_e32 v138, v162
	s_add_i32 s80, s83, s17
	global_load_lds_dwordx4 v[214:215], off
	s_mov_b32 m0, s80
	s_nop 0
	global_load_lds_dwordx4 v138, s[6:7]
	v_mov_b32_e32 v138, v164
	s_add_i32 m0, s80, 0x2000
	s_nop 0
	global_load_lds_dwordx4 v138, s[6:7]
	v_mov_b32_e32 v138, v1
	s_mov_b32 m0, s64
	v_lshl_add_u64 v[214:215], s[4:5], 0, v[138:139]
	v_lshl_add_u64 v[214:215], v[214:215], 0, s[12:13]
	v_mov_b32_e32 v138, v163
	global_load_lds_dwordx4 v[214:215], off
	s_mov_b32 m0, s65
	v_lshl_add_u64 v[214:215], s[4:5], 0, v[138:139]
	v_lshl_add_u64 v[214:215], v[214:215], 0, s[12:13]
	global_load_lds_dwordx4 v[214:215], off
	s_waitcnt vmcnt(8)
	s_waitcnt lgkmcnt(0)
	s_barrier
	s_setprio 1
	s_waitcnt lgkmcnt(0)
	v_mfma_f32_16x16x32_bf16 v[62:65], v[130:133], v[178:181], v[62:65]
	v_mfma_f32_16x16x32_bf16 v[58:61], v[142:145], v[178:181], v[58:61]
	v_mfma_f32_16x16x32_bf16 v[46:49], v[130:133], v[186:189], v[46:49]
	v_mfma_f32_16x16x32_bf16 v[42:45], v[142:145], v[186:189], v[42:45]
	v_mfma_f32_16x16x32_bf16 v[30:33], v[130:133], v[194:197], v[30:33]
	v_mfma_f32_16x16x32_bf16 v[26:29], v[142:145], v[194:197], v[26:29]
	v_mfma_f32_16x16x32_bf16 v[14:17], v[130:133], v[204:207], v[14:17]
	v_mfma_f32_16x16x32_bf16 v[10:13], v[142:145], v[204:207], v[10:13]
	v_mfma_f32_16x16x32_bf16 v[62:65], v[134:137], v[182:185], v[62:65]
	v_mfma_f32_16x16x32_bf16 v[58:61], v[146:149], v[182:185], v[58:61]
	v_mfma_f32_16x16x32_bf16 v[46:49], v[134:137], v[190:193], v[46:49]
	v_mfma_f32_16x16x32_bf16 v[42:45], v[146:149], v[190:193], v[42:45]
	v_mfma_f32_16x16x32_bf16 v[30:33], v[134:137], v[200:203], v[30:33]
	v_mfma_f32_16x16x32_bf16 v[26:29], v[146:149], v[200:203], v[26:29]
	v_mfma_f32_16x16x32_bf16 v[14:17], v[134:137], v[208:211], v[14:17]
	v_mfma_f32_16x16x32_bf16 v[10:13], v[146:149], v[208:211], v[10:13]
	s_setprio 0
	s_setprio 1
	v_mfma_f32_16x16x32_bf16 v[54:57], v[150:153], v[178:181], v[54:57]
	v_mfma_f32_16x16x32_bf16 v[50:53], v[158:161], v[178:181], v[50:53]
	v_mfma_f32_16x16x32_bf16 v[38:41], v[150:153], v[186:189], v[38:41]
	v_mfma_f32_16x16x32_bf16 v[34:37], v[158:161], v[186:189], v[34:37]
	v_mfma_f32_16x16x32_bf16 v[22:25], v[150:153], v[194:197], v[22:25]
	v_mfma_f32_16x16x32_bf16 v[18:21], v[158:161], v[194:197], v[18:21]
	v_mfma_f32_16x16x32_bf16 v[6:9], v[150:153], v[204:207], v[6:9]
	v_mfma_f32_16x16x32_bf16 v[2:5], v[158:161], v[204:207], v[2:5]
	v_mfma_f32_16x16x32_bf16 v[54:57], v[154:157], v[182:185], v[54:57]
	v_mfma_f32_16x16x32_bf16 v[50:53], v[174:177], v[182:185], v[50:53]
	v_mfma_f32_16x16x32_bf16 v[38:41], v[154:157], v[190:193], v[38:41]
	v_mfma_f32_16x16x32_bf16 v[34:37], v[174:177], v[190:193], v[34:37]
	v_mfma_f32_16x16x32_bf16 v[22:25], v[154:157], v[200:203], v[22:25]
	v_mfma_f32_16x16x32_bf16 v[18:21], v[174:177], v[200:203], v[18:21]
	v_mfma_f32_16x16x32_bf16 v[6:9], v[154:157], v[208:211], v[6:9]
	v_mfma_f32_16x16x32_bf16 v[2:5], v[174:177], v[208:211], v[2:5]
	s_setprio 0
	s_barrier
	s_add_i32 s79, s79, 2
	s_add_u32 s0, s0, 0x100
	s_addc_u32 s1, s1, 0
	s_add_u32 s77, s77, 0x100
	s_addc_u32 s78, s78, 0
	s_cmp_gt_u32 s79, 29
	s_cbranch_scc0 .LBB5_802
	s_and_b64 vcc, exec, s[18:19]
	s_cbranch_vccz .LBB5_805
	s_barrier
